# grid-barrier and queue spin loops poll every s_sleep 2 (was 4)
# speedup vs baseline: 1.0029x; 1.0029x over previous
; __device__ __forceinline__ unsigned xb_ld(unsigned* p)              { return __hip_atomic_load(p, __ATOMIC_RELAXED, __HIP_MEMORY_SCOPE_AGENT); }
; __device__ __forceinline__ void xcd_barrier_complete(unsigned* bar, unsigned x, unsigned& nloc, unsigned& nx) {
;     ...
;     for (;;) {
;         sum = 0u; cnt = 0u; mine = 0u;
; #pragma unroll
;         for (unsigned j = 0; j < 16; ++j) { const unsigned c = xb_ld(&bar[XB_XCNT(j)]); sum += c; cnt += (c > 0u) ? 1u : 0u; mine = (j == x) ? c : mine; }
;         if (sum == G) break;
;         __builtin_amdgcn_s_sleep(1);
;         if ((++sp & 255u) == 0u) { if (xb_ld(&bar[XB_TMO])) break; if (sp > XB_SPIN_CAP) { atomicAdd(&bar[XB_TMO], 1u); break; } }
;     }
.LBB0_136:
	global_load_dword v16, v17, s[8:9] sc1
	global_load_dword v1, v17, s[10:11] sc1
	global_load_dword v2, v17, s[14:15] sc1
	global_load_dword v3, v17, s[36:37] sc1
	global_load_dword v4, v17, s[38:39] sc1
	global_load_dword v5, v17, s[40:41] sc1
	global_load_dword v6, v17, s[42:43] sc1
	global_load_dword v7, v17, s[48:49] sc1
	global_load_dword v8, v17, s[50:51] sc1
	global_load_dword v9, v17, s[56:57] sc1
	global_load_dword v10, v17, s[58:59] sc1
	global_load_dword v11, v17, s[60:61] sc1
	global_load_dword v12, v17, s[62:63] sc1
	global_load_dword v13, v17, s[64:65] sc1
	global_load_dword v14, v17, s[66:67] sc1
	global_load_dword v15, v17, s[68:69] sc1
	s_mov_b64 s[70:71], -1
	s_mov_b64 s[72:73], -1
	s_waitcnt vmcnt(14)
	v_add_u32_e32 v18, v1, v16
	s_waitcnt vmcnt(13)
	v_add_u32_e32 v18, v18, v2
	s_waitcnt vmcnt(12)
	v_add_u32_e32 v18, v18, v3
	s_waitcnt vmcnt(11)
	v_add_u32_e32 v18, v18, v4
	s_waitcnt vmcnt(10)
	v_add_u32_e32 v18, v18, v5
	s_waitcnt vmcnt(9)
	v_add_u32_e32 v18, v18, v6
	s_waitcnt vmcnt(8)
	v_add_u32_e32 v18, v18, v7
	s_waitcnt vmcnt(7)
	v_add_u32_e32 v18, v18, v8
	s_waitcnt vmcnt(6)
	v_add_u32_e32 v18, v18, v9
	s_waitcnt vmcnt(5)
	v_add_u32_e32 v18, v18, v10
	s_waitcnt vmcnt(4)
	v_add_u32_e32 v18, v18, v11
	s_waitcnt vmcnt(3)
	v_add_u32_e32 v18, v18, v12
	s_waitcnt vmcnt(2)
	v_add_u32_e32 v18, v18, v13
	s_waitcnt vmcnt(1)
	v_add_u32_e32 v18, v18, v14
	s_waitcnt vmcnt(0)
	v_add_u32_e32 v18, v18, v15
	v_cmp_eq_u32_e32 vcc, s3, v18
	s_cbranch_vccnz .LBB0_135
	s_and_b32 s35, s34, 0xff
	s_cmp_eq_u32 s35, 0
	s_mov_b64 s[74:75], -1
	s_sleep 2
	s_cbranch_scc1 .LBB0_140
	s_and_b64 vcc, exec, s[74:75]
	s_cbranch_vccz .LBB0_135

.LBB0_152:
	s_and_b32 s34, s3, 0xff
	s_mov_b64 s[42:43], -1
	s_cmp_lg_u32 s34, 0
	s_mov_b64 s[50:51], -1
	s_sleep 2
	s_cbranch_scc0 .LBB0_155
	s_and_b64 vcc, exec, s[50:51]
	s_cbranch_vccz .LBB0_151

.LBB0_169:
	s_and_b32 s34, s3, 0xff
	s_cmp_lg_u32 s34, 0
	s_mov_b64 s[48:49], -1
	s_sleep 2
	s_cbranch_scc0 .LBB0_172
	s_mov_b64 s[50:51], -1
	s_and_b64 vcc, exec, s[48:49]
	s_cbranch_vccz .LBB0_168

; __device__ __forceinline__ unsigned xb_ld(unsigned* p)              { return __hip_atomic_load(p, __ATOMIC_RELAXED, __HIP_MEMORY_SCOPE_AGENT); }
; __device__ __forceinline__ void xcd_barrier_complete(unsigned* bar, unsigned x, unsigned& nloc, unsigned& nx) {
;     ...
;     for (;;) {
;         sum = 0u; cnt = 0u; mine = 0u;
; #pragma unroll
;         for (unsigned j = 0; j < 16; ++j) { const unsigned c = xb_ld(&bar[XB_XCNT(j)]); sum += c; cnt += (c > 0u) ? 1u : 0u; mine = (j == x) ? c : mine; }
;         if (sum == G) break;
;         __builtin_amdgcn_s_sleep(1);
;         if ((++sp & 255u) == 0u) { if (xb_ld(&bar[XB_TMO])) break; if (sp > XB_SPIN_CAP) { atomicAdd(&bar[XB_TMO], 1u); break; } }
;     }
.LBB0_320:
	global_load_dword v16, v17, s[8:9] sc1
	global_load_dword v1, v17, s[10:11] sc1
	global_load_dword v2, v17, s[14:15] sc1
	global_load_dword v3, v17, s[36:37] sc1
	global_load_dword v4, v17, s[38:39] sc1
	global_load_dword v5, v17, s[40:41] sc1
	global_load_dword v6, v17, s[42:43] sc1
	global_load_dword v7, v17, s[44:45] sc1
	global_load_dword v8, v17, s[48:49] sc1
	global_load_dword v9, v17, s[50:51] sc1
	global_load_dword v10, v17, s[56:57] sc1
	global_load_dword v11, v17, s[58:59] sc1
	global_load_dword v12, v17, s[60:61] sc1
	global_load_dword v13, v17, s[62:63] sc1
	global_load_dword v14, v17, s[64:65] sc1
	global_load_dword v15, v17, s[66:67] sc1
	s_mov_b64 s[68:69], -1
	s_mov_b64 s[70:71], -1
	s_waitcnt vmcnt(14)
	v_add_u32_e32 v18, v1, v16
	s_waitcnt vmcnt(13)
	v_add_u32_e32 v18, v18, v2
	s_waitcnt vmcnt(12)
	v_add_u32_e32 v18, v18, v3
	s_waitcnt vmcnt(11)
	v_add_u32_e32 v18, v18, v4
	s_waitcnt vmcnt(10)
	v_add_u32_e32 v18, v18, v5
	s_waitcnt vmcnt(9)
	v_add_u32_e32 v18, v18, v6
	s_waitcnt vmcnt(8)
	v_add_u32_e32 v18, v18, v7
	s_waitcnt vmcnt(7)
	v_add_u32_e32 v18, v18, v8
	s_waitcnt vmcnt(6)
	v_add_u32_e32 v18, v18, v9
	s_waitcnt vmcnt(5)
	v_add_u32_e32 v18, v18, v10
	s_waitcnt vmcnt(4)
	v_add_u32_e32 v18, v18, v11
	s_waitcnt vmcnt(3)
	v_add_u32_e32 v18, v18, v12
	s_waitcnt vmcnt(2)
	v_add_u32_e32 v18, v18, v13
	s_waitcnt vmcnt(1)
	v_add_u32_e32 v18, v18, v14
	s_waitcnt vmcnt(0)
	v_add_u32_e32 v18, v18, v15
	v_cmp_eq_u32_e32 vcc, s3, v18
	s_cbranch_vccnz .LBB0_319
	s_and_b32 s35, s34, 0xff
	s_cmp_eq_u32 s35, 0
	s_mov_b64 s[72:73], -1
	s_sleep 2
	s_cbranch_scc1 .LBB0_324
	s_and_b64 vcc, exec, s[72:73]
	s_cbranch_vccz .LBB0_319

.LBB0_336:
	s_and_b32 s34, s3, 0xff
	s_mov_b64 s[42:43], -1
	s_cmp_lg_u32 s34, 0
	s_mov_b64 s[48:49], -1
	s_sleep 2
	s_cbranch_scc0 .LBB0_339
	s_and_b64 vcc, exec, s[48:49]
	s_cbranch_vccz .LBB0_335

.LBB0_353:
	s_and_b32 s34, s3, 0xff
	s_cmp_lg_u32 s34, 0
	s_mov_b64 s[44:45], -1
	s_sleep 2
	s_cbranch_scc0 .LBB0_356
	s_mov_b64 s[48:49], -1
	s_and_b64 vcc, exec, s[44:45]
	s_cbranch_vccz .LBB0_352

; __device__ __forceinline__ unsigned xb_ld(unsigned* p)              { return __hip_atomic_load(p, __ATOMIC_RELAXED, __HIP_MEMORY_SCOPE_AGENT); }
; __device__ __forceinline__ void xcd_barrier_complete(unsigned* bar, unsigned x, unsigned& nloc, unsigned& nx) {
;     ...
;     for (;;) {
;         sum = 0u; cnt = 0u; mine = 0u;
; #pragma unroll
;         for (unsigned j = 0; j < 16; ++j) { const unsigned c = xb_ld(&bar[XB_XCNT(j)]); sum += c; cnt += (c > 0u) ? 1u : 0u; mine = (j == x) ? c : mine; }
;         if (sum == G) break;
;         __builtin_amdgcn_s_sleep(1);
;         if ((++sp & 255u) == 0u) { if (xb_ld(&bar[XB_TMO])) break; if (sp > XB_SPIN_CAP) { atomicAdd(&bar[XB_TMO], 1u); break; } }
;     }
.LBB0_723:
	global_load_dword v16, v17, s[8:9] sc1
	global_load_dword v1, v17, s[10:11] sc1
	global_load_dword v2, v17, s[14:15] sc1
	global_load_dword v3, v17, s[36:37] sc1
	global_load_dword v4, v17, s[38:39] sc1
	global_load_dword v5, v17, s[40:41] sc1
	global_load_dword v6, v17, s[42:43] sc1
	global_load_dword v7, v17, s[44:45] sc1
	global_load_dword v8, v17, s[46:47] sc1
	global_load_dword v9, v17, s[48:49] sc1
	global_load_dword v10, v17, s[50:51] sc1
	global_load_dword v11, v17, s[56:57] sc1
	global_load_dword v12, v17, s[58:59] sc1
	global_load_dword v13, v17, s[60:61] sc1
	global_load_dword v14, v17, s[62:63] sc1
	global_load_dword v15, v17, s[64:65] sc1
	s_mov_b64 s[66:67], -1
	s_mov_b64 s[68:69], -1
	s_waitcnt vmcnt(14)
	v_add_u32_e32 v18, v1, v16
	s_waitcnt vmcnt(13)
	v_add_u32_e32 v18, v18, v2
	s_waitcnt vmcnt(12)
	v_add_u32_e32 v18, v18, v3
	s_waitcnt vmcnt(11)
	v_add_u32_e32 v18, v18, v4
	s_waitcnt vmcnt(10)
	v_add_u32_e32 v18, v18, v5
	s_waitcnt vmcnt(9)
	v_add_u32_e32 v18, v18, v6
	s_waitcnt vmcnt(8)
	v_add_u32_e32 v18, v18, v7
	s_waitcnt vmcnt(7)
	v_add_u32_e32 v18, v18, v8
	s_waitcnt vmcnt(6)
	v_add_u32_e32 v18, v18, v9
	s_waitcnt vmcnt(5)
	v_add_u32_e32 v18, v18, v10
	s_waitcnt vmcnt(4)
	v_add_u32_e32 v18, v18, v11
	s_waitcnt vmcnt(3)
	v_add_u32_e32 v18, v18, v12
	s_waitcnt vmcnt(2)
	v_add_u32_e32 v18, v18, v13
	s_waitcnt vmcnt(1)
	v_add_u32_e32 v18, v18, v14
	s_waitcnt vmcnt(0)
	v_add_u32_e32 v18, v18, v15
	v_cmp_eq_u32_e32 vcc, s3, v18
	s_cbranch_vccnz .LBB0_722
	s_and_b32 s35, s34, 0xff
	s_cmp_eq_u32 s35, 0
	s_mov_b64 s[70:71], -1
	s_sleep 2
	s_cbranch_scc1 .LBB0_727
	s_and_b64 vcc, exec, s[70:71]
	s_cbranch_vccz .LBB0_722

.LBB0_739:
	s_and_b32 s34, s3, 0xff
	s_mov_b64 s[42:43], -1
	s_cmp_lg_u32 s34, 0
	s_mov_b64 s[46:47], -1
	s_sleep 2
	s_cbranch_scc0 .LBB0_742
	s_and_b64 vcc, exec, s[46:47]
	s_cbranch_vccz .LBB0_738

.LBB0_756:
	s_and_b32 s34, s3, 0xff
	s_cmp_lg_u32 s34, 0
	s_mov_b64 s[44:45], -1
	s_sleep 2
	s_cbranch_scc0 .LBB0_759
	s_mov_b64 s[46:47], -1
	s_and_b64 vcc, exec, s[44:45]
	s_cbranch_vccz .LBB0_755

; __device__ __forceinline__ unsigned xb_ld(unsigned* p)              { return __hip_atomic_load(p, __ATOMIC_RELAXED, __HIP_MEMORY_SCOPE_AGENT); }
; __device__ __forceinline__ void xcd_barrier_complete(unsigned* bar, unsigned x, unsigned& nloc, unsigned& nx) {
;     ...
;     for (;;) {
;         sum = 0u; cnt = 0u; mine = 0u;
; #pragma unroll
;         for (unsigned j = 0; j < 16; ++j) { const unsigned c = xb_ld(&bar[XB_XCNT(j)]); sum += c; cnt += (c > 0u) ? 1u : 0u; mine = (j == x) ? c : mine; }
;         if (sum == G) break;
;         __builtin_amdgcn_s_sleep(1);
;         if ((++sp & 255u) == 0u) { if (xb_ld(&bar[XB_TMO])) break; if (sp > XB_SPIN_CAP) { atomicAdd(&bar[XB_TMO], 1u); break; } }
;     }
.LBB0_958:
	global_load_dword v16, v17, s[6:7] sc1
	global_load_dword v1, v17, s[8:9] sc1
	global_load_dword v2, v17, s[10:11] sc1
	global_load_dword v3, v17, s[12:13] sc1
	global_load_dword v4, v17, s[14:15] sc1
	global_load_dword v5, v17, s[18:19] sc1
	global_load_dword v6, v17, s[36:37] sc1
	global_load_dword v7, v17, s[38:39] sc1
	global_load_dword v8, v17, s[40:41] sc1
	global_load_dword v9, v17, s[42:43] sc1
	global_load_dword v10, v17, s[44:45] sc1
	global_load_dword v11, v17, s[46:47] sc1
	global_load_dword v12, v17, s[48:49] sc1
	global_load_dword v13, v17, s[50:51] sc1
	global_load_dword v14, v17, s[56:57] sc1
	global_load_dword v15, v17, s[58:59] sc1
	s_mov_b64 s[60:61], -1
	s_mov_b64 s[62:63], -1
	s_waitcnt vmcnt(14)
	v_add_u32_e32 v18, v1, v16
	s_waitcnt vmcnt(13)
	v_add_u32_e32 v18, v18, v2
	s_waitcnt vmcnt(12)
	v_add_u32_e32 v18, v18, v3
	s_waitcnt vmcnt(11)
	v_add_u32_e32 v18, v18, v4
	s_waitcnt vmcnt(10)
	v_add_u32_e32 v18, v18, v5
	s_waitcnt vmcnt(9)
	v_add_u32_e32 v18, v18, v6
	s_waitcnt vmcnt(8)
	v_add_u32_e32 v18, v18, v7
	s_waitcnt vmcnt(7)
	v_add_u32_e32 v18, v18, v8
	s_waitcnt vmcnt(6)
	v_add_u32_e32 v18, v18, v9
	s_waitcnt vmcnt(5)
	v_add_u32_e32 v18, v18, v10
	s_waitcnt vmcnt(4)
	v_add_u32_e32 v18, v18, v11
	s_waitcnt vmcnt(3)
	v_add_u32_e32 v18, v18, v12
	s_waitcnt vmcnt(2)
	v_add_u32_e32 v18, v18, v13
	s_waitcnt vmcnt(1)
	v_add_u32_e32 v18, v18, v14
	s_waitcnt vmcnt(0)
	v_add_u32_e32 v18, v18, v15
	v_cmp_eq_u32_e32 vcc, s3, v18
	s_cbranch_vccnz .LBB0_957
	s_and_b32 s35, s34, 0xff
	s_cmp_eq_u32 s35, 0
	s_mov_b64 s[64:65], -1
	s_sleep 2
	s_cbranch_scc1 .LBB0_962
	s_and_b64 vcc, exec, s[64:65]
	s_cbranch_vccz .LBB0_957

.LBB0_974:
	s_and_b32 s34, s3, 0xff
	s_mov_b64 s[36:37], -1
	s_cmp_lg_u32 s34, 0
	s_mov_b64 s[40:41], -1
	s_sleep 2
	s_cbranch_scc0 .LBB0_977
	s_and_b64 vcc, exec, s[40:41]
	s_cbranch_vccz .LBB0_973

.LBB0_991:
	s_and_b32 s34, s3, 0xff
	s_cmp_lg_u32 s34, 0
	s_mov_b64 s[38:39], -1
	s_sleep 2
	s_cbranch_scc0 .LBB0_994
	s_mov_b64 s[40:41], -1
	s_and_b64 vcc, exec, s[38:39]
	s_cbranch_vccz .LBB0_990

; __device__ __forceinline__ unsigned xb_ld(unsigned* p)              { return __hip_atomic_load(p, __ATOMIC_RELAXED, __HIP_MEMORY_SCOPE_AGENT); }
; __device__ __forceinline__ void xcd_barrier_complete(unsigned* bar, unsigned x, unsigned& nloc, unsigned& nx) {
;     ...
;     for (;;) {
;         sum = 0u; cnt = 0u; mine = 0u;
; #pragma unroll
;         for (unsigned j = 0; j < 16; ++j) { const unsigned c = xb_ld(&bar[XB_XCNT(j)]); sum += c; cnt += (c > 0u) ? 1u : 0u; mine = (j == x) ? c : mine; }
;         if (sum == G) break;
;         __builtin_amdgcn_s_sleep(1);
;         if ((++sp & 255u) == 0u) { if (xb_ld(&bar[XB_TMO])) break; if (sp > XB_SPIN_CAP) { atomicAdd(&bar[XB_TMO], 1u); break; } }
;     }
.LBB0_1053:
	global_load_dword v16, v17, s[6:7] sc1
	global_load_dword v1, v17, s[8:9] sc1
	global_load_dword v2, v17, s[10:11] sc1
	global_load_dword v3, v17, s[12:13] sc1
	global_load_dword v4, v17, s[14:15] sc1
	global_load_dword v5, v17, s[18:19] sc1
	global_load_dword v6, v17, s[36:37] sc1
	global_load_dword v7, v17, s[38:39] sc1
	global_load_dword v8, v17, s[40:41] sc1
	global_load_dword v9, v17, s[42:43] sc1
	global_load_dword v10, v17, s[44:45] sc1
	global_load_dword v11, v17, s[46:47] sc1
	global_load_dword v12, v17, s[48:49] sc1
	global_load_dword v13, v17, s[50:51] sc1
	global_load_dword v14, v17, s[56:57] sc1
	global_load_dword v15, v17, s[58:59] sc1
	s_mov_b64 s[60:61], -1
	s_mov_b64 s[62:63], -1
	s_waitcnt vmcnt(14)
	v_add_u32_e32 v18, v1, v16
	s_waitcnt vmcnt(13)
	v_add_u32_e32 v18, v18, v2
	s_waitcnt vmcnt(12)
	v_add_u32_e32 v18, v18, v3
	s_waitcnt vmcnt(11)
	v_add_u32_e32 v18, v18, v4
	s_waitcnt vmcnt(10)
	v_add_u32_e32 v18, v18, v5
	s_waitcnt vmcnt(9)
	v_add_u32_e32 v18, v18, v6
	s_waitcnt vmcnt(8)
	v_add_u32_e32 v18, v18, v7
	s_waitcnt vmcnt(7)
	v_add_u32_e32 v18, v18, v8
	s_waitcnt vmcnt(6)
	v_add_u32_e32 v18, v18, v9
	s_waitcnt vmcnt(5)
	v_add_u32_e32 v18, v18, v10
	s_waitcnt vmcnt(4)
	v_add_u32_e32 v18, v18, v11
	s_waitcnt vmcnt(3)
	v_add_u32_e32 v18, v18, v12
	s_waitcnt vmcnt(2)
	v_add_u32_e32 v18, v18, v13
	s_waitcnt vmcnt(1)
	v_add_u32_e32 v18, v18, v14
	s_waitcnt vmcnt(0)
	v_add_u32_e32 v18, v18, v15
	v_cmp_eq_u32_e32 vcc, s34, v18
	s_cbranch_vccnz .LBB0_1052
	s_and_b32 s53, s35, 0xff
	s_cmp_eq_u32 s53, 0
	s_mov_b64 s[64:65], -1
	s_sleep 2
	s_cbranch_scc1 .LBB0_1057
	s_and_b64 vcc, exec, s[64:65]
	s_cbranch_vccz .LBB0_1052

.LBB0_1069:
	s_and_b32 s35, s34, 0xff
	s_mov_b64 s[36:37], -1
	s_cmp_lg_u32 s35, 0
	s_mov_b64 s[40:41], -1
	s_sleep 2
	s_cbranch_scc0 .LBB0_1072
	s_and_b64 vcc, exec, s[40:41]
	s_cbranch_vccz .LBB0_1068

.LBB0_1086:
	s_and_b32 s35, s34, 0xff
	s_cmp_lg_u32 s35, 0
	s_mov_b64 s[38:39], -1
	s_sleep 2
	s_cbranch_scc0 .LBB0_1089
	s_mov_b64 s[40:41], -1
	s_and_b64 vcc, exec, s[38:39]
	s_cbranch_vccz .LBB0_1085

; __device__ __forceinline__ unsigned xb_ld(unsigned* p)              { return __hip_atomic_load(p, __ATOMIC_RELAXED, __HIP_MEMORY_SCOPE_AGENT); }
; __device__ __forceinline__ void xcd_barrier_complete(unsigned* bar, unsigned x, unsigned& nloc, unsigned& nx) {
;     ...
;     for (;;) {
;         sum = 0u; cnt = 0u; mine = 0u;
; #pragma unroll
;         for (unsigned j = 0; j < 16; ++j) { const unsigned c = xb_ld(&bar[XB_XCNT(j)]); sum += c; cnt += (c > 0u) ? 1u : 0u; mine = (j == x) ? c : mine; }
;         if (sum == G) break;
;         __builtin_amdgcn_s_sleep(1);
;         if ((++sp & 255u) == 0u) { if (xb_ld(&bar[XB_TMO])) break; if (sp > XB_SPIN_CAP) { atomicAdd(&bar[XB_TMO], 1u); break; } }
;     }
.LBB0_1114:
	global_load_dword v16, v17, s[6:7] sc1
	global_load_dword v1, v17, s[8:9] sc1
	global_load_dword v2, v17, s[10:11] sc1
	global_load_dword v3, v17, s[12:13] sc1
	global_load_dword v4, v17, s[14:15] sc1
	global_load_dword v5, v17, s[16:17] sc1
	global_load_dword v6, v17, s[18:19] sc1
	global_load_dword v7, v17, s[36:37] sc1
	global_load_dword v8, v17, s[38:39] sc1
	global_load_dword v9, v17, s[40:41] sc1
	global_load_dword v10, v17, s[42:43] sc1
	global_load_dword v11, v17, s[44:45] sc1
	global_load_dword v12, v17, s[46:47] sc1
	global_load_dword v13, v17, s[48:49] sc1
	global_load_dword v14, v17, s[50:51] sc1
	global_load_dword v15, v17, s[56:57] sc1
	s_mov_b64 s[58:59], -1
	s_mov_b64 s[60:61], -1
	s_waitcnt vmcnt(14)
	v_add_u32_e32 v18, v1, v16
	s_waitcnt vmcnt(13)
	v_add_u32_e32 v18, v18, v2
	s_waitcnt vmcnt(12)
	v_add_u32_e32 v18, v18, v3
	s_waitcnt vmcnt(11)
	v_add_u32_e32 v18, v18, v4
	s_waitcnt vmcnt(10)
	v_add_u32_e32 v18, v18, v5
	s_waitcnt vmcnt(9)
	v_add_u32_e32 v18, v18, v6
	s_waitcnt vmcnt(8)
	v_add_u32_e32 v18, v18, v7
	s_waitcnt vmcnt(7)
	v_add_u32_e32 v18, v18, v8
	s_waitcnt vmcnt(6)
	v_add_u32_e32 v18, v18, v9
	s_waitcnt vmcnt(5)
	v_add_u32_e32 v18, v18, v10
	s_waitcnt vmcnt(4)
	v_add_u32_e32 v18, v18, v11
	s_waitcnt vmcnt(3)
	v_add_u32_e32 v18, v18, v12
	s_waitcnt vmcnt(2)
	v_add_u32_e32 v18, v18, v13
	s_waitcnt vmcnt(1)
	v_add_u32_e32 v18, v18, v14
	s_waitcnt vmcnt(0)
	v_add_u32_e32 v18, v18, v15
	v_cmp_eq_u32_e32 vcc, s34, v18
	s_cbranch_vccnz .LBB0_1113
	s_and_b32 s53, s35, 0xff
	s_cmp_eq_u32 s53, 0
	s_mov_b64 s[62:63], -1
	s_sleep 2
	s_cbranch_scc1 .LBB0_1118
	s_and_b64 vcc, exec, s[62:63]
	s_cbranch_vccz .LBB0_1113

.LBB0_1130:
	s_and_b32 s35, s34, 0xff
	s_mov_b64 s[18:19], -1
	s_cmp_lg_u32 s35, 0
	s_mov_b64 s[38:39], -1
	s_sleep 2
	s_cbranch_scc0 .LBB0_1133
	s_and_b64 vcc, exec, s[38:39]
	s_cbranch_vccz .LBB0_1129

.LBB0_1147:
	s_and_b32 s18, s34, 0xff
	s_cmp_lg_u32 s18, 0
	s_mov_b64 s[36:37], -1
	s_sleep 2
	s_cbranch_scc0 .LBB0_1150
	s_mov_b64 s[38:39], -1
	s_and_b64 vcc, exec, s[36:37]
	s_cbranch_vccz .LBB0_1146

; __device__ __forceinline__ unsigned xb_ld(unsigned* p)              { return __hip_atomic_load(p, __ATOMIC_RELAXED, __HIP_MEMORY_SCOPE_AGENT); }
; __device__ __forceinline__ void xcd_barrier_complete(unsigned* bar, unsigned x, unsigned& nloc, unsigned& nx) {
;     ...
;     for (;;) {
;         sum = 0u; cnt = 0u; mine = 0u;
; #pragma unroll
;         for (unsigned j = 0; j < 16; ++j) { const unsigned c = xb_ld(&bar[XB_XCNT(j)]); sum += c; cnt += (c > 0u) ? 1u : 0u; mine = (j == x) ? c : mine; }
;         if (sum == G) break;
;         __builtin_amdgcn_s_sleep(1);
;         if ((++sp & 255u) == 0u) { if (xb_ld(&bar[XB_TMO])) break; if (sp > XB_SPIN_CAP) { atomicAdd(&bar[XB_TMO], 1u); break; } }
;     }
.LBB0_1220:
	global_load_dword v16, v17, s[6:7] sc1
	global_load_dword v1, v17, s[8:9] sc1
	global_load_dword v2, v17, s[10:11] sc1
	global_load_dword v3, v17, s[12:13] sc1
	global_load_dword v4, v17, s[14:15] sc1
	global_load_dword v5, v17, s[16:17] sc1
	global_load_dword v6, v17, s[18:19] sc1
	global_load_dword v7, v17, s[20:21] sc1
	global_load_dword v8, v17, s[36:37] sc1
	global_load_dword v9, v17, s[38:39] sc1
	global_load_dword v10, v17, s[40:41] sc1
	global_load_dword v11, v17, s[42:43] sc1
	global_load_dword v12, v17, s[44:45] sc1
	global_load_dword v13, v17, s[46:47] sc1
	global_load_dword v14, v17, s[48:49] sc1
	global_load_dword v15, v17, s[50:51] sc1
	s_mov_b64 s[56:57], -1
	s_mov_b64 s[58:59], -1
	s_waitcnt vmcnt(14)
	v_add_u32_e32 v18, v1, v16
	s_waitcnt vmcnt(13)
	v_add_u32_e32 v18, v18, v2
	s_waitcnt vmcnt(12)
	v_add_u32_e32 v18, v18, v3
	s_waitcnt vmcnt(11)
	v_add_u32_e32 v18, v18, v4
	s_waitcnt vmcnt(10)
	v_add_u32_e32 v18, v18, v5
	s_waitcnt vmcnt(9)
	v_add_u32_e32 v18, v18, v6
	s_waitcnt vmcnt(8)
	v_add_u32_e32 v18, v18, v7
	s_waitcnt vmcnt(7)
	v_add_u32_e32 v18, v18, v8
	s_waitcnt vmcnt(6)
	v_add_u32_e32 v18, v18, v9
	s_waitcnt vmcnt(5)
	v_add_u32_e32 v18, v18, v10
	s_waitcnt vmcnt(4)
	v_add_u32_e32 v18, v18, v11
	s_waitcnt vmcnt(3)
	v_add_u32_e32 v18, v18, v12
	s_waitcnt vmcnt(2)
	v_add_u32_e32 v18, v18, v13
	s_waitcnt vmcnt(1)
	v_add_u32_e32 v18, v18, v14
	s_waitcnt vmcnt(0)
	v_add_u32_e32 v18, v18, v15
	v_cmp_eq_u32_e32 vcc, s34, v18
	s_cbranch_vccnz .LBB0_1219
	s_and_b32 s53, s35, 0xff
	s_cmp_eq_u32 s53, 0
	s_mov_b64 s[60:61], -1
	s_sleep 2
	s_cbranch_scc1 .LBB0_1224
	s_and_b64 vcc, exec, s[60:61]
	s_cbranch_vccz .LBB0_1219

.LBB0_1236:
	s_and_b32 s20, s34, 0xff
	s_mov_b64 s[18:19], -1
	s_cmp_lg_u32 s20, 0
	s_mov_b64 s[36:37], -1
	s_sleep 2
	s_cbranch_scc0 .LBB0_1239
	s_and_b64 vcc, exec, s[36:37]
	s_cbranch_vccz .LBB0_1235

.LBB0_1253:
	s_and_b32 s18, s34, 0xff
	s_cmp_lg_u32 s18, 0
	s_mov_b64 s[20:21], -1
	s_sleep 2
	s_cbranch_scc0 .LBB0_1256
	s_mov_b64 s[36:37], -1
	s_and_b64 vcc, exec, s[20:21]
	s_cbranch_vccz .LBB0_1252

; #define VM_WAIT() asm volatile("s_waitcnt vmcnt(0)" ::: "memory")
; __device__ __forceinline__ unsigned xb_ld(unsigned* p)              { return __hip_atomic_load(p, __ATOMIC_RELAXED, __HIP_MEMORY_SCOPE_AGENT); }
; #define XB_SPIN(cond, bar) do { unsigned _sp = 0; while (cond) { __builtin_amdgcn_s_sleep(1); \
;     if ((++_sp & 255u) == 0u) { if (xb_ld(&(bar)[XB_TMO])) break; if (_sp > XB_SPIN_CAP) { atomicAdd(&(bar)[XB_TMO], 1u); break; } } } } while (0)
; __global__ void __launch_bounds__(NTHREADS, 2) mk_fwd(Args args) {
;     ...
;                     if (F.tid == 0) { unsigned* bw = (unsigned*)(F.ctl + CW_BAR); XB_SPIN(xb_ld((unsigned*)(F.ctl + CW_CVT9)) < (unsigned)nconv, bw); __builtin_amdgcn_fence(__ATOMIC_ACQUIRE, "agent"); VM_WAIT(); }
;                     __syncthreads();
.LBB0_1302:
	s_and_b32 s36, s40, 0xff
	s_mov_b64 s[22:23], -1
	s_cmp_lg_u32 s36, 0
	s_mov_b64 s[38:39], -1
	s_sleep 2
	s_cbranch_scc0 .LBB0_1305
	s_and_b64 vcc, exec, s[38:39]
	s_cbranch_vccz .LBB0_1301

; __device__ __forceinline__ unsigned xb_ld(unsigned* p)              { return __hip_atomic_load(p, __ATOMIC_RELAXED, __HIP_MEMORY_SCOPE_AGENT); }
; __device__ __forceinline__ void xcd_barrier_complete(unsigned* bar, unsigned x, unsigned& nloc, unsigned& nx) {
;     ...
;     for (;;) {
;         sum = 0u; cnt = 0u; mine = 0u;
; #pragma unroll
;         for (unsigned j = 0; j < 16; ++j) { const unsigned c = xb_ld(&bar[XB_XCNT(j)]); sum += c; cnt += (c > 0u) ? 1u : 0u; mine = (j == x) ? c : mine; }
;         if (sum == G) break;
;         __builtin_amdgcn_s_sleep(1);
;         if ((++sp & 255u) == 0u) { if (xb_ld(&bar[XB_TMO])) break; if (sp > XB_SPIN_CAP) { atomicAdd(&bar[XB_TMO], 1u); break; } }
;     }
.LBB0_1356:
	global_load_dword v15, v16, s[6:7] sc1
	global_load_dword v0, v16, s[8:9] sc1
	global_load_dword v1, v16, s[10:11] sc1
	global_load_dword v2, v16, s[12:13] sc1
	global_load_dword v3, v16, s[14:15] sc1
	global_load_dword v4, v16, s[16:17] sc1
	global_load_dword v5, v16, s[18:19] sc1
	global_load_dword v6, v16, s[20:21] sc1
	global_load_dword v7, v16, s[22:23] sc1
	global_load_dword v8, v16, s[24:25] sc1
	global_load_dword v9, v16, s[36:37] sc1
	global_load_dword v10, v16, s[38:39] sc1
	global_load_dword v11, v16, s[40:41] sc1
	global_load_dword v12, v16, s[42:43] sc1
	global_load_dword v13, v16, s[44:45] sc1
	global_load_dword v14, v16, s[46:47] sc1
	s_mov_b64 s[48:49], -1
	s_mov_b64 s[50:51], -1
	s_waitcnt vmcnt(14)
	v_add_u32_e32 v17, v0, v15
	s_waitcnt vmcnt(13)
	v_add_u32_e32 v17, v17, v1
	s_waitcnt vmcnt(12)
	v_add_u32_e32 v17, v17, v2
	s_waitcnt vmcnt(11)
	v_add_u32_e32 v17, v17, v3
	s_waitcnt vmcnt(10)
	v_add_u32_e32 v17, v17, v4
	s_waitcnt vmcnt(9)
	v_add_u32_e32 v17, v17, v5
	s_waitcnt vmcnt(8)
	v_add_u32_e32 v17, v17, v6
	s_waitcnt vmcnt(7)
	v_add_u32_e32 v17, v17, v7
	s_waitcnt vmcnt(6)
	v_add_u32_e32 v17, v17, v8
	s_waitcnt vmcnt(5)
	v_add_u32_e32 v17, v17, v9
	s_waitcnt vmcnt(4)
	v_add_u32_e32 v17, v17, v10
	s_waitcnt vmcnt(3)
	v_add_u32_e32 v17, v17, v11
	s_waitcnt vmcnt(2)
	v_add_u32_e32 v17, v17, v12
	s_waitcnt vmcnt(1)
	v_add_u32_e32 v17, v17, v13
	s_waitcnt vmcnt(0)
	v_add_u32_e32 v17, v17, v14
	v_cmp_eq_u32_e32 vcc, s34, v17
	s_cbranch_vccnz .LBB0_1355
	s_and_b32 s48, s35, 0xff
	s_cmp_eq_u32 s48, 0
	s_mov_b64 s[48:49], -1
	s_mov_b64 s[54:55], -1
	s_sleep 2
	s_cbranch_scc1 .LBB0_1360
	s_and_b64 vcc, exec, s[54:55]
	s_cbranch_vccz .LBB0_1355

.LBB0_1372:
	s_and_b32 s20, s24, 0xff
	s_mov_b64 s[18:19], -1
	s_cmp_lg_u32 s20, 0
	s_mov_b64 s[22:23], -1
	s_sleep 2
	s_cbranch_scc0 .LBB0_1375
	s_and_b64 vcc, exec, s[22:23]
	s_cbranch_vccz .LBB0_1371

.LBB0_1389:
	s_and_b32 s18, s24, 0xff
	s_cmp_lg_u32 s18, 0
	s_mov_b64 s[20:21], -1
	s_sleep 2
	s_cbranch_scc0 .LBB0_1392
	s_mov_b64 s[22:23], -1
	s_and_b64 vcc, exec, s[20:21]
	s_cbranch_vccz .LBB0_1388
